# GEMM K-loops: SP1 MFMA block moved back between its two barriers (hipcc had sunk it below the 2nd barrier) in the 4 full-tile fp8 GEMM loops
# speedup vs baseline: 1.0248x; 1.0248x over previous
.LBB0_497:
	s_cmpk_eq_i32 s26, 0x300
	s_cselect_b64 s[28:29], -1, 0
	s_add_i32 s23, 0, 0x10000
	v_add_u32_e32 v0, s23, v205
	s_add_i32 s30, 0, 0x14000
	v_add_u32_e32 v1, s23, v237
	ds_read_b128 v[8:11], v0
	ds_read_b128 v[12:15], v1
	v_add_u32_e32 v0, s76, v205
	v_add_u32_e32 v1, s76, v237
	ds_read_b128 v[24:27], v0
	ds_read_b128 v[28:31], v1
	v_add_u32_e32 v0, s30, v205
	v_add_u32_e32 v4, s30, v237
	v_add_u32_e32 v16, s77, v205
	v_add_u32_e32 v20, s77, v237
	ds_read_b128 v[0:3], v0
	ds_read_b128 v[4:7], v4
	ds_read_b128 v[16:19], v16
	ds_read_b128 v[20:23], v20
	s_add_i32 m0, s49, 0xc000
	s_add_u32 s30, s46, s26
	s_addc_u32 s31, s9, s27
	s_add_i32 s23, s49, 0xe000
	s_cmpk_lg_i32 s26, 0x300
	ds_read_b128 v[40:43], v239
	ds_read_b128 v[32:35], v239 offset:2048
	ds_read_b128 v[44:47], v240
	ds_read_b128 v[36:39], v240 offset:2048
	ds_read_b128 v[56:59], v239 offset:4096
	ds_read_b128 v[48:51], v239 offset:6144
	ds_read_b128 v[60:63], v240 offset:4096
	ds_read_b128 v[52:55], v240 offset:6144
	global_load_lds_dwordx4 v96, s[30:31]
	s_mov_b32 m0, s23
	s_nop 0
	global_load_lds_dwordx4 v206, s[30:31]
	s_waitcnt vmcnt(8)
	s_waitcnt lgkmcnt(0)
	s_barrier
	s_setprio 1
	s_waitcnt lgkmcnt(0)
	v_mfma_scale_f32_16x16x128_f8f6f4 v[190:193], v[8:15], v[40:47], v[190:193], v226, v225 op_sel_hi:[0,0,0]
	v_mfma_scale_f32_16x16x128_f8f6f4 v[186:189], v[24:31], v[40:47], v[186:189], v226, v225 op_sel_hi:[0,0,0]
	v_mfma_scale_f32_16x16x128_f8f6f4 v[174:177], v[8:15], v[32:39], v[174:177], v226, v225 op_sel_hi:[0,0,0]
	v_mfma_scale_f32_16x16x128_f8f6f4 v[170:173], v[24:31], v[32:39], v[170:173], v226, v225 op_sel_hi:[0,0,0]
	v_mfma_scale_f32_16x16x128_f8f6f4 v[158:161], v[8:15], v[56:63], v[158:161], v226, v225 op_sel_hi:[0,0,0]
	v_mfma_scale_f32_16x16x128_f8f6f4 v[154:157], v[24:31], v[56:63], v[154:157], v226, v225 op_sel_hi:[0,0,0]
	v_mfma_scale_f32_16x16x128_f8f6f4 v[142:145], v[8:15], v[48:55], v[142:145], v226, v225 op_sel_hi:[0,0,0]
	v_mfma_scale_f32_16x16x128_f8f6f4 v[138:141], v[24:31], v[48:55], v[138:141], v226, v225 op_sel_hi:[0,0,0]
	s_setprio 0
	s_setprio 1
	v_mfma_scale_f32_16x16x128_f8f6f4 v[182:185], v[0:7], v[40:47], v[182:185], v226, v225 op_sel_hi:[0,0,0]
	v_mfma_scale_f32_16x16x128_f8f6f4 v[178:181], v[16:23], v[40:47], v[178:181], v226, v225 op_sel_hi:[0,0,0]
	v_mfma_scale_f32_16x16x128_f8f6f4 v[166:169], v[0:7], v[32:39], v[166:169], v226, v225 op_sel_hi:[0,0,0]
	v_mfma_scale_f32_16x16x128_f8f6f4 v[162:165], v[16:23], v[32:39], v[162:165], v226, v225 op_sel_hi:[0,0,0]
	v_mfma_scale_f32_16x16x128_f8f6f4 v[150:153], v[0:7], v[56:63], v[150:153], v226, v225 op_sel_hi:[0,0,0]
	v_mfma_scale_f32_16x16x128_f8f6f4 v[146:149], v[16:23], v[56:63], v[146:149], v226, v225 op_sel_hi:[0,0,0]
	v_mfma_scale_f32_16x16x128_f8f6f4 v[134:137], v[0:7], v[48:55], v[134:137], v226, v225 op_sel_hi:[0,0,0]
	v_mfma_scale_f32_16x16x128_f8f6f4 v[130:133], v[16:23], v[48:55], v[130:133], v226, v225 op_sel_hi:[0,0,0]
	s_setprio 0
	s_barrier
	s_cbranch_scc1 .LBB0_499
	v_mov_b64_e32 v[212:213], v[210:211]
	v_mov_b64_e32 v[214:215], v[208:209]
	v_mov_b32_e32 v206, v210
	v_mov_b32_e32 v96, v208
	v_mov_b32_e32 v204, v243
	v_mov_b32_e32 v202, v224
	v_mov_b32_e32 v241, v210
	v_mov_b32_e32 v242, v208
	s_branch .LBB0_500

.LBB0_500:
	s_and_b64 s[30:31], s[24:25], s[28:29]
	s_add_i32 s23, s5, 2
	s_and_b64 s[28:29], s[28:29], exec
	s_cselect_b32 s96, 0, s23
	s_and_b64 s[28:29], s[30:31], exec
	s_cselect_b32 s28, s52, s4
	s_ashr_i32 s29, s28, 31
	s_lshl_b64 s[30:31], s[96:97], 7
	s_or_b32 s96, s96, 1
	s_lshl_b64 s[34:35], s[28:29], 18
	s_lshl_b64 s[28:29], s[96:97], 7
	s_add_u32 s72, s6, s34
	s_addc_u32 s73, s7, s35
	s_add_u32 s34, s72, s30
	s_addc_u32 s35, s73, s31
	v_lshl_add_u64 v[216:217], s[34:35], 0, v[194:195]
	s_mov_b32 m0, s56
	ds_read_b128 v[56:59], v239 offset:16384
	ds_read_b128 v[60:63], v240 offset:16384
	ds_read_b128 v[48:51], v239 offset:18432
	ds_read_b128 v[52:55], v240 offset:18432
	ds_read_b128 v[40:43], v239 offset:20480
	ds_read_b128 v[44:47], v240 offset:20480
	ds_read_b128 v[32:35], v239 offset:22528
	ds_read_b128 v[36:39], v240 offset:22528
	global_load_lds_dwordx4 v[216:217], off
	v_lshl_add_u64 v[216:217], s[34:35], 0, v[196:197]
	s_add_u32 s34, s34, 0x20000
	s_mov_b32 m0, s57
	s_addc_u32 s35, s35, 0
	global_load_lds_dwordx4 v[216:217], off
	v_lshl_add_u64 v[216:217], s[34:35], 0, v[194:195]
	s_mov_b32 m0, s58
	s_add_u32 s30, s78, s30
	global_load_lds_dwordx4 v[216:217], off
	v_lshl_add_u64 v[216:217], s[34:35], 0, v[196:197]
	s_mov_b32 m0, s59
	s_addc_u32 s31, s79, s31
	global_load_lds_dwordx4 v[216:217], off
	s_mov_b32 m0, s49
	s_nop 0
	global_load_lds_dwordx4 v202, s[30:31]
	s_mov_b32 m0, s60
	s_nop 0
	global_load_lds_dwordx4 v204, s[30:31]
	s_waitcnt vmcnt(8)
	s_waitcnt lgkmcnt(0)
	s_barrier
	s_setprio 1
	s_waitcnt lgkmcnt(0)
	v_mfma_scale_f32_16x16x128_f8f6f4 v[126:129], v[8:15], v[56:63], v[126:129], v226, v225 op_sel_hi:[0,0,0]
	v_mfma_scale_f32_16x16x128_f8f6f4 v[122:125], v[24:31], v[56:63], v[122:125], v226, v225 op_sel_hi:[0,0,0]
	v_mfma_scale_f32_16x16x128_f8f6f4 v[110:113], v[8:15], v[48:55], v[110:113], v226, v225 op_sel_hi:[0,0,0]
	v_mfma_scale_f32_16x16x128_f8f6f4 v[106:109], v[24:31], v[48:55], v[106:109], v226, v225 op_sel_hi:[0,0,0]
	v_mfma_scale_f32_16x16x128_f8f6f4 v[92:95], v[8:15], v[40:47], v[92:95], v226, v225 op_sel_hi:[0,0,0]
	v_mfma_scale_f32_16x16x128_f8f6f4 v[88:91], v[24:31], v[40:47], v[88:91], v226, v225 op_sel_hi:[0,0,0]
	v_mfma_scale_f32_16x16x128_f8f6f4 v[76:79], v[8:15], v[32:39], v[76:79], v226, v225 op_sel_hi:[0,0,0]
	v_mfma_scale_f32_16x16x128_f8f6f4 v[72:75], v[24:31], v[32:39], v[72:75], v226, v225 op_sel_hi:[0,0,0]
	s_setprio 0
	s_setprio 1
	v_mfma_scale_f32_16x16x128_f8f6f4 v[118:121], v[0:7], v[56:63], v[118:121], v226, v225 op_sel_hi:[0,0,0]
	v_mfma_scale_f32_16x16x128_f8f6f4 v[114:117], v[16:23], v[56:63], v[114:117], v226, v225 op_sel_hi:[0,0,0]
	v_mfma_scale_f32_16x16x128_f8f6f4 v[102:105], v[0:7], v[48:55], v[102:105], v226, v225 op_sel_hi:[0,0,0]
	v_mfma_scale_f32_16x16x128_f8f6f4 v[98:101], v[16:23], v[48:55], v[98:101], v226, v225 op_sel_hi:[0,0,0]
	v_mfma_scale_f32_16x16x128_f8f6f4 v[84:87], v[0:7], v[40:47], v[84:87], v226, v225 op_sel_hi:[0,0,0]
	v_mfma_scale_f32_16x16x128_f8f6f4 v[80:83], v[16:23], v[40:47], v[80:83], v226, v225 op_sel_hi:[0,0,0]
	v_mfma_scale_f32_16x16x128_f8f6f4 v[68:71], v[0:7], v[32:39], v[68:71], v226, v225 op_sel_hi:[0,0,0]
	v_mfma_scale_f32_16x16x128_f8f6f4 v[64:67], v[16:23], v[32:39], v[64:67], v226, v225 op_sel_hi:[0,0,0]
	s_setprio 0
	s_barrier
	s_add_i32 s34, 0, 0x18000
	s_add_i32 s35, 0, 0x1c000
	v_add_u32_e32 v0, s34, v205
	v_add_u32_e32 v4, s34, v237
	v_add_u32_e32 v8, s94, v205
	v_add_u32_e32 v12, s94, v237
	v_add_u32_e32 v16, s35, v205
	v_add_u32_e32 v20, s35, v237
	v_add_u32_e32 v24, s33, v205
	v_add_u32_e32 v28, s33, v237
	ds_read_b128 v[0:3], v0
	ds_read_b128 v[4:7], v4
	ds_read_b128 v[8:11], v8
	ds_read_b128 v[12:15], v12
	ds_read_b128 v[16:19], v16
	ds_read_b128 v[20:23], v20
	ds_read_b128 v[24:27], v24
	ds_read_b128 v[28:31], v28
	s_mov_b32 m0, s61
	v_lshl_add_u64 v[214:215], s[30:31], 0, v[214:215]
	ds_read_b128 v[32:35], v239 offset:32768
	ds_read_b128 v[40:43], v239 offset:34816
	ds_read_b128 v[36:39], v240 offset:32768
	ds_read_b128 v[44:47], v240 offset:34816
	ds_read_b128 v[48:51], v239 offset:36864
	ds_read_b128 v[56:59], v239 offset:38912
	ds_read_b128 v[52:55], v240 offset:36864
	ds_read_b128 v[60:63], v240 offset:38912
	global_load_lds_dwordx4 v[214:215], off
	v_lshl_add_u64 v[212:213], s[30:31], 0, v[212:213]
	s_mov_b32 m0, s64
	s_nop 0
	global_load_lds_dwordx4 v[212:213], off
	s_waitcnt vmcnt(8)
	s_waitcnt lgkmcnt(0)
	s_barrier
	s_setprio 1
	s_waitcnt lgkmcnt(0)
	v_mfma_scale_f32_16x16x128_f8f6f4 v[190:193], v[0:7], v[32:39], v[190:193], v226, v225 op_sel_hi:[0,0,0]
	v_mfma_scale_f32_16x16x128_f8f6f4 v[186:189], v[8:15], v[32:39], v[186:189], v226, v225 op_sel_hi:[0,0,0]
	v_mfma_scale_f32_16x16x128_f8f6f4 v[174:177], v[0:7], v[40:47], v[174:177], v226, v225 op_sel_hi:[0,0,0]
	v_mfma_scale_f32_16x16x128_f8f6f4 v[170:173], v[8:15], v[40:47], v[170:173], v226, v225 op_sel_hi:[0,0,0]
	v_mfma_scale_f32_16x16x128_f8f6f4 v[158:161], v[0:7], v[48:55], v[158:161], v226, v225 op_sel_hi:[0,0,0]
	v_mfma_scale_f32_16x16x128_f8f6f4 v[154:157], v[8:15], v[48:55], v[154:157], v226, v225 op_sel_hi:[0,0,0]
	v_mfma_scale_f32_16x16x128_f8f6f4 v[142:145], v[0:7], v[56:63], v[142:145], v226, v225 op_sel_hi:[0,0,0]
	v_mfma_scale_f32_16x16x128_f8f6f4 v[138:141], v[8:15], v[56:63], v[138:141], v226, v225 op_sel_hi:[0,0,0]
	s_setprio 0
	s_setprio 1
	v_mfma_scale_f32_16x16x128_f8f6f4 v[182:185], v[16:23], v[32:39], v[182:185], v226, v225 op_sel_hi:[0,0,0]
	v_mfma_scale_f32_16x16x128_f8f6f4 v[178:181], v[24:31], v[32:39], v[178:181], v226, v225 op_sel_hi:[0,0,0]
	v_mfma_scale_f32_16x16x128_f8f6f4 v[166:169], v[16:23], v[40:47], v[166:169], v226, v225 op_sel_hi:[0,0,0]
	v_mfma_scale_f32_16x16x128_f8f6f4 v[162:165], v[24:31], v[40:47], v[162:165], v226, v225 op_sel_hi:[0,0,0]
	v_mfma_scale_f32_16x16x128_f8f6f4 v[150:153], v[16:23], v[48:55], v[150:153], v226, v225 op_sel_hi:[0,0,0]
	v_mfma_scale_f32_16x16x128_f8f6f4 v[146:149], v[24:31], v[48:55], v[146:149], v226, v225 op_sel_hi:[0,0,0]
	v_mfma_scale_f32_16x16x128_f8f6f4 v[134:137], v[16:23], v[56:63], v[134:137], v226, v225 op_sel_hi:[0,0,0]
	v_mfma_scale_f32_16x16x128_f8f6f4 v[130:133], v[24:31], v[56:63], v[130:133], v226, v225 op_sel_hi:[0,0,0]
	s_setprio 0
	s_barrier
	s_add_u32 s30, s72, s28
	s_addc_u32 s31, s73, s29
	s_add_i32 s34, s34, s48
	v_lshl_add_u64 v[212:213], s[30:31], 0, v[194:195]
	s_mov_b32 m0, s34
	ds_read_b128 v[32:35], v239 offset:49152
	ds_read_b128 v[40:43], v239 offset:51200
	ds_read_b128 v[36:39], v240 offset:49152
	ds_read_b128 v[44:47], v240 offset:51200
	ds_read_b128 v[48:51], v239 offset:53248
	ds_read_b128 v[56:59], v239 offset:55296
	ds_read_b128 v[52:55], v240 offset:53248
	ds_read_b128 v[60:63], v240 offset:55296
	global_load_lds_dwordx4 v[212:213], off
	s_add_i32 m0, s34, 0x2000
	v_lshl_add_u64 v[212:213], s[30:31], 0, v[196:197]
	s_add_u32 s30, s30, 0x20000
	s_addc_u32 s31, s31, 0
	s_add_i32 s34, s35, s48
	global_load_lds_dwordx4 v[212:213], off
	v_lshl_add_u64 v[212:213], s[30:31], 0, v[194:195]
	s_mov_b32 m0, s34
	s_nop 0
	global_load_lds_dwordx4 v[212:213], off
	s_add_i32 m0, s34, 0x2000
	v_lshl_add_u64 v[212:213], s[30:31], 0, v[196:197]
	s_add_u32 s28, s78, s28
	global_load_lds_dwordx4 v[212:213], off
	s_addc_u32 s29, s79, s29
	s_mov_b32 m0, s65
	s_nop 0
	global_load_lds_dwordx4 v202, s[28:29]
	s_mov_b32 m0, s92
	s_nop 0
	global_load_lds_dwordx4 v204, s[28:29]
	s_waitcnt vmcnt(8)
	s_waitcnt lgkmcnt(0)
	s_barrier
	s_setprio 1
	s_waitcnt lgkmcnt(0)
	v_mfma_scale_f32_16x16x128_f8f6f4 v[126:129], v[0:7], v[32:39], v[126:129], v226, v225 op_sel_hi:[0,0,0]
	v_mfma_scale_f32_16x16x128_f8f6f4 v[122:125], v[8:15], v[32:39], v[122:125], v226, v225 op_sel_hi:[0,0,0]
	v_mfma_scale_f32_16x16x128_f8f6f4 v[110:113], v[0:7], v[40:47], v[110:113], v226, v225 op_sel_hi:[0,0,0]
	v_mfma_scale_f32_16x16x128_f8f6f4 v[106:109], v[8:15], v[40:47], v[106:109], v226, v225 op_sel_hi:[0,0,0]
	v_mfma_scale_f32_16x16x128_f8f6f4 v[92:95], v[0:7], v[48:55], v[92:95], v226, v225 op_sel_hi:[0,0,0]
	v_mfma_scale_f32_16x16x128_f8f6f4 v[88:91], v[8:15], v[48:55], v[88:91], v226, v225 op_sel_hi:[0,0,0]
	v_mfma_scale_f32_16x16x128_f8f6f4 v[76:79], v[0:7], v[56:63], v[76:79], v226, v225 op_sel_hi:[0,0,0]
	v_mfma_scale_f32_16x16x128_f8f6f4 v[72:75], v[8:15], v[56:63], v[72:75], v226, v225 op_sel_hi:[0,0,0]
	s_setprio 0
	s_setprio 1
	v_mfma_scale_f32_16x16x128_f8f6f4 v[118:121], v[16:23], v[32:39], v[118:121], v226, v225 op_sel_hi:[0,0,0]
	v_mfma_scale_f32_16x16x128_f8f6f4 v[114:117], v[24:31], v[32:39], v[114:117], v226, v225 op_sel_hi:[0,0,0]
	v_mfma_scale_f32_16x16x128_f8f6f4 v[102:105], v[16:23], v[40:47], v[102:105], v226, v225 op_sel_hi:[0,0,0]
	v_mfma_scale_f32_16x16x128_f8f6f4 v[98:101], v[24:31], v[40:47], v[98:101], v226, v225 op_sel_hi:[0,0,0]
	v_mfma_scale_f32_16x16x128_f8f6f4 v[84:87], v[16:23], v[48:55], v[84:87], v226, v225 op_sel_hi:[0,0,0]
	v_mfma_scale_f32_16x16x128_f8f6f4 v[80:83], v[24:31], v[48:55], v[80:83], v226, v225 op_sel_hi:[0,0,0]
	v_mfma_scale_f32_16x16x128_f8f6f4 v[68:71], v[16:23], v[56:63], v[68:71], v226, v225 op_sel_hi:[0,0,0]
	v_mfma_scale_f32_16x16x128_f8f6f4 v[64:67], v[24:31], v[56:63], v[64:67], v226, v225 op_sel_hi:[0,0,0]
	s_setprio 0
	s_barrier
	s_add_u32 s26, s26, 0x100
	s_addc_u32 s27, s27, 0
	s_cmp_gt_u32 s5, 5
	s_cbranch_scc1 .LBB0_502
	s_mov_b32 s5, s23
	s_branch .LBB0_497

.LBB0_986:
	s_cmpk_eq_i32 s10, 0x300
	s_cselect_b64 s[12:13], -1, 0
	s_add_i32 s14, 0, 0x10000
	v_add_u32_e32 v0, s14, v205
	s_add_i32 s15, 0, 0x14000
	v_add_u32_e32 v1, s14, v237
	ds_read_b128 v[8:11], v0
	ds_read_b128 v[12:15], v1
	v_add_u32_e32 v0, s76, v205
	v_add_u32_e32 v1, s76, v237
	ds_read_b128 v[24:27], v0
	ds_read_b128 v[28:31], v1
	v_add_u32_e32 v0, s15, v205
	v_add_u32_e32 v4, s15, v237
	v_add_u32_e32 v16, s77, v205
	v_add_u32_e32 v20, s77, v237
	ds_read_b128 v[0:3], v0
	ds_read_b128 v[4:7], v4
	ds_read_b128 v[16:19], v16
	ds_read_b128 v[20:23], v20
	s_add_i32 m0, s21, 0xc000
	s_add_u32 s14, s41, s10
	s_addc_u32 s15, s45, s11
	s_add_i32 s16, s21, 0xe000
	s_cmpk_lg_i32 s10, 0x300
	ds_read_b128 v[40:43], v239
	ds_read_b128 v[32:35], v239 offset:2048
	ds_read_b128 v[44:47], v240
	ds_read_b128 v[36:39], v240 offset:2048
	ds_read_b128 v[56:59], v239 offset:4096
	ds_read_b128 v[48:51], v239 offset:6144
	ds_read_b128 v[60:63], v240 offset:4096
	ds_read_b128 v[52:55], v240 offset:6144
	global_load_lds_dwordx4 v96, s[14:15]
	s_mov_b32 m0, s16
	s_nop 0
	global_load_lds_dwordx4 v206, s[14:15]
	s_waitcnt vmcnt(8)
	s_waitcnt lgkmcnt(0)
	s_barrier
	s_setprio 1
	s_waitcnt lgkmcnt(0)
	v_mfma_scale_f32_16x16x128_f8f6f4 v[186:189], v[8:15], v[40:47], v[186:189], v226, v225 op_sel_hi:[0,0,0]
	v_mfma_scale_f32_16x16x128_f8f6f4 v[190:193], v[24:31], v[40:47], v[190:193], v226, v225 op_sel_hi:[0,0,0]
	v_mfma_scale_f32_16x16x128_f8f6f4 v[174:177], v[8:15], v[32:39], v[174:177], v226, v225 op_sel_hi:[0,0,0]
	v_mfma_scale_f32_16x16x128_f8f6f4 v[170:173], v[24:31], v[32:39], v[170:173], v226, v225 op_sel_hi:[0,0,0]
	v_mfma_scale_f32_16x16x128_f8f6f4 v[158:161], v[8:15], v[56:63], v[158:161], v226, v225 op_sel_hi:[0,0,0]
	v_mfma_scale_f32_16x16x128_f8f6f4 v[154:157], v[24:31], v[56:63], v[154:157], v226, v225 op_sel_hi:[0,0,0]
	v_mfma_scale_f32_16x16x128_f8f6f4 v[142:145], v[8:15], v[48:55], v[142:145], v226, v225 op_sel_hi:[0,0,0]
	v_mfma_scale_f32_16x16x128_f8f6f4 v[138:141], v[24:31], v[48:55], v[138:141], v226, v225 op_sel_hi:[0,0,0]
	s_setprio 0
	s_setprio 1
	v_mfma_scale_f32_16x16x128_f8f6f4 v[182:185], v[0:7], v[40:47], v[182:185], v226, v225 op_sel_hi:[0,0,0]
	v_mfma_scale_f32_16x16x128_f8f6f4 v[178:181], v[16:23], v[40:47], v[178:181], v226, v225 op_sel_hi:[0,0,0]
	v_mfma_scale_f32_16x16x128_f8f6f4 v[166:169], v[0:7], v[32:39], v[166:169], v226, v225 op_sel_hi:[0,0,0]
	v_mfma_scale_f32_16x16x128_f8f6f4 v[162:165], v[16:23], v[32:39], v[162:165], v226, v225 op_sel_hi:[0,0,0]
	v_mfma_scale_f32_16x16x128_f8f6f4 v[150:153], v[0:7], v[56:63], v[150:153], v226, v225 op_sel_hi:[0,0,0]
	v_mfma_scale_f32_16x16x128_f8f6f4 v[146:149], v[16:23], v[56:63], v[146:149], v226, v225 op_sel_hi:[0,0,0]
	v_mfma_scale_f32_16x16x128_f8f6f4 v[134:137], v[0:7], v[48:55], v[134:137], v226, v225 op_sel_hi:[0,0,0]
	v_mfma_scale_f32_16x16x128_f8f6f4 v[130:133], v[16:23], v[48:55], v[130:133], v226, v225 op_sel_hi:[0,0,0]
	s_setprio 0
	s_barrier
	s_cbranch_scc1 .LBB0_988
	v_mov_b64_e32 v[212:213], v[210:211]
	v_mov_b64_e32 v[214:215], v[208:209]
	v_mov_b32_e32 v206, v210
	v_mov_b32_e32 v96, v208
	v_mov_b32_e32 v204, v243
	v_mov_b32_e32 v202, v224
	v_mov_b32_e32 v241, v210
	v_mov_b32_e32 v242, v208
	s_branch .LBB0_989

.LBB0_989:
	s_and_b64 s[14:15], s[8:9], s[12:13]
	s_add_i32 s52, s49, 2
	s_and_b64 s[12:13], s[12:13], exec
	s_cselect_b32 s96, 0, s52
	s_and_b64 s[12:13], s[14:15], exec
	s_cselect_b32 s12, s47, s23
	s_ashr_i32 s13, s12, 31
	s_lshl_b64 s[14:15], s[96:97], 7
	s_or_b32 s96, s96, 1
	s_lshl_b64 s[16:17], s[12:13], 18
	s_lshl_b64 s[12:13], s[96:97], 7
	s_add_u32 s53, s18, s16
	s_addc_u32 s54, s19, s17
	s_add_u32 s16, s53, s14
	s_addc_u32 s17, s54, s15
	v_lshl_add_u64 v[216:217], s[16:17], 0, v[194:195]
	s_mov_b32 m0, s24
	ds_read_b128 v[56:59], v239 offset:16384
	ds_read_b128 v[60:63], v240 offset:16384
	ds_read_b128 v[48:51], v239 offset:18432
	ds_read_b128 v[52:55], v240 offset:18432
	ds_read_b128 v[40:43], v239 offset:20480
	ds_read_b128 v[44:47], v240 offset:20480
	ds_read_b128 v[32:35], v239 offset:22528
	ds_read_b128 v[36:39], v240 offset:22528
	global_load_lds_dwordx4 v[216:217], off
	v_lshl_add_u64 v[216:217], s[16:17], 0, v[196:197]
	s_add_u32 s16, s16, 0x20000
	s_mov_b32 m0, s25
	s_addc_u32 s17, s17, 0
	global_load_lds_dwordx4 v[216:217], off
	v_lshl_add_u64 v[216:217], s[16:17], 0, v[194:195]
	s_mov_b32 m0, s26
	s_add_u32 s14, s78, s14
	global_load_lds_dwordx4 v[216:217], off
	v_lshl_add_u64 v[216:217], s[16:17], 0, v[196:197]
	s_mov_b32 m0, s27
	s_addc_u32 s15, s79, s15
	global_load_lds_dwordx4 v[216:217], off
	s_mov_b32 m0, s21
	s_nop 0
	global_load_lds_dwordx4 v202, s[14:15]
	s_mov_b32 m0, s28
	s_nop 0
	global_load_lds_dwordx4 v204, s[14:15]
	s_waitcnt vmcnt(8)
	s_waitcnt lgkmcnt(0)
	s_barrier
	s_setprio 1
	s_waitcnt lgkmcnt(0)
	v_mfma_scale_f32_16x16x128_f8f6f4 v[126:129], v[8:15], v[56:63], v[126:129], v226, v225 op_sel_hi:[0,0,0]
	v_mfma_scale_f32_16x16x128_f8f6f4 v[122:125], v[24:31], v[56:63], v[122:125], v226, v225 op_sel_hi:[0,0,0]
	v_mfma_scale_f32_16x16x128_f8f6f4 v[110:113], v[8:15], v[48:55], v[110:113], v226, v225 op_sel_hi:[0,0,0]
	v_mfma_scale_f32_16x16x128_f8f6f4 v[106:109], v[24:31], v[48:55], v[106:109], v226, v225 op_sel_hi:[0,0,0]
	v_mfma_scale_f32_16x16x128_f8f6f4 v[92:95], v[8:15], v[40:47], v[92:95], v226, v225 op_sel_hi:[0,0,0]
	v_mfma_scale_f32_16x16x128_f8f6f4 v[88:91], v[24:31], v[40:47], v[88:91], v226, v225 op_sel_hi:[0,0,0]
	v_mfma_scale_f32_16x16x128_f8f6f4 v[76:79], v[8:15], v[32:39], v[76:79], v226, v225 op_sel_hi:[0,0,0]
	v_mfma_scale_f32_16x16x128_f8f6f4 v[72:75], v[24:31], v[32:39], v[72:75], v226, v225 op_sel_hi:[0,0,0]
	s_setprio 0
	s_setprio 1
	v_mfma_scale_f32_16x16x128_f8f6f4 v[118:121], v[0:7], v[56:63], v[118:121], v226, v225 op_sel_hi:[0,0,0]
	v_mfma_scale_f32_16x16x128_f8f6f4 v[114:117], v[16:23], v[56:63], v[114:117], v226, v225 op_sel_hi:[0,0,0]
	v_mfma_scale_f32_16x16x128_f8f6f4 v[102:105], v[0:7], v[48:55], v[102:105], v226, v225 op_sel_hi:[0,0,0]
	v_mfma_scale_f32_16x16x128_f8f6f4 v[98:101], v[16:23], v[48:55], v[98:101], v226, v225 op_sel_hi:[0,0,0]
	v_mfma_scale_f32_16x16x128_f8f6f4 v[84:87], v[0:7], v[40:47], v[84:87], v226, v225 op_sel_hi:[0,0,0]
	v_mfma_scale_f32_16x16x128_f8f6f4 v[80:83], v[16:23], v[40:47], v[80:83], v226, v225 op_sel_hi:[0,0,0]
	v_mfma_scale_f32_16x16x128_f8f6f4 v[68:71], v[0:7], v[32:39], v[68:71], v226, v225 op_sel_hi:[0,0,0]
	v_mfma_scale_f32_16x16x128_f8f6f4 v[64:67], v[16:23], v[32:39], v[64:67], v226, v225 op_sel_hi:[0,0,0]
	s_setprio 0
	s_barrier
	s_add_i32 s16, 0, 0x18000
	s_add_i32 s17, 0, 0x1c000
	v_add_u32_e32 v0, s16, v205
	v_add_u32_e32 v4, s16, v237
	v_add_u32_e32 v8, s94, v205
	v_add_u32_e32 v12, s94, v237
	v_add_u32_e32 v16, s17, v205
	v_add_u32_e32 v20, s17, v237
	v_add_u32_e32 v24, s33, v205
	v_add_u32_e32 v28, s33, v237
	ds_read_b128 v[0:3], v0
	ds_read_b128 v[4:7], v4
	ds_read_b128 v[8:11], v8
	ds_read_b128 v[12:15], v12
	ds_read_b128 v[16:19], v16
	ds_read_b128 v[20:23], v20
	ds_read_b128 v[24:27], v24
	ds_read_b128 v[28:31], v28
	s_mov_b32 m0, s29
	v_lshl_add_u64 v[214:215], s[14:15], 0, v[214:215]
	ds_read_b128 v[32:35], v239 offset:32768
	ds_read_b128 v[40:43], v239 offset:34816
	ds_read_b128 v[36:39], v240 offset:32768
	ds_read_b128 v[44:47], v240 offset:34816
	ds_read_b128 v[48:51], v239 offset:36864
	ds_read_b128 v[56:59], v239 offset:38912
	ds_read_b128 v[52:55], v240 offset:36864
	ds_read_b128 v[60:63], v240 offset:38912
	global_load_lds_dwordx4 v[214:215], off
	v_lshl_add_u64 v[212:213], s[14:15], 0, v[212:213]
	s_mov_b32 m0, s30
	s_nop 0
	global_load_lds_dwordx4 v[212:213], off
	s_waitcnt vmcnt(8)
	s_waitcnt lgkmcnt(0)
	s_barrier
	s_setprio 1
	s_waitcnt lgkmcnt(0)
	v_mfma_scale_f32_16x16x128_f8f6f4 v[186:189], v[0:7], v[32:39], v[186:189], v226, v225 op_sel_hi:[0,0,0]
	v_mfma_scale_f32_16x16x128_f8f6f4 v[190:193], v[8:15], v[32:39], v[190:193], v226, v225 op_sel_hi:[0,0,0]
	v_mfma_scale_f32_16x16x128_f8f6f4 v[174:177], v[0:7], v[40:47], v[174:177], v226, v225 op_sel_hi:[0,0,0]
	v_mfma_scale_f32_16x16x128_f8f6f4 v[170:173], v[8:15], v[40:47], v[170:173], v226, v225 op_sel_hi:[0,0,0]
	v_mfma_scale_f32_16x16x128_f8f6f4 v[158:161], v[0:7], v[48:55], v[158:161], v226, v225 op_sel_hi:[0,0,0]
	v_mfma_scale_f32_16x16x128_f8f6f4 v[154:157], v[8:15], v[48:55], v[154:157], v226, v225 op_sel_hi:[0,0,0]
	v_mfma_scale_f32_16x16x128_f8f6f4 v[142:145], v[0:7], v[56:63], v[142:145], v226, v225 op_sel_hi:[0,0,0]
	v_mfma_scale_f32_16x16x128_f8f6f4 v[138:141], v[8:15], v[56:63], v[138:141], v226, v225 op_sel_hi:[0,0,0]
	s_setprio 0
	s_setprio 1
	v_mfma_scale_f32_16x16x128_f8f6f4 v[182:185], v[16:23], v[32:39], v[182:185], v226, v225 op_sel_hi:[0,0,0]
	v_mfma_scale_f32_16x16x128_f8f6f4 v[178:181], v[24:31], v[32:39], v[178:181], v226, v225 op_sel_hi:[0,0,0]
	v_mfma_scale_f32_16x16x128_f8f6f4 v[166:169], v[16:23], v[40:47], v[166:169], v226, v225 op_sel_hi:[0,0,0]
	v_mfma_scale_f32_16x16x128_f8f6f4 v[162:165], v[24:31], v[40:47], v[162:165], v226, v225 op_sel_hi:[0,0,0]
	v_mfma_scale_f32_16x16x128_f8f6f4 v[150:153], v[16:23], v[48:55], v[150:153], v226, v225 op_sel_hi:[0,0,0]
	v_mfma_scale_f32_16x16x128_f8f6f4 v[146:149], v[24:31], v[48:55], v[146:149], v226, v225 op_sel_hi:[0,0,0]
	v_mfma_scale_f32_16x16x128_f8f6f4 v[134:137], v[16:23], v[56:63], v[134:137], v226, v225 op_sel_hi:[0,0,0]
	v_mfma_scale_f32_16x16x128_f8f6f4 v[130:133], v[24:31], v[56:63], v[130:133], v226, v225 op_sel_hi:[0,0,0]
	s_setprio 0
	s_barrier
	s_add_u32 s14, s53, s12
	s_addc_u32 s15, s54, s13
	s_add_i32 s16, s16, s20
	v_lshl_add_u64 v[212:213], s[14:15], 0, v[194:195]
	s_mov_b32 m0, s16
	ds_read_b128 v[32:35], v239 offset:49152
	ds_read_b128 v[40:43], v239 offset:51200
	ds_read_b128 v[36:39], v240 offset:49152
	ds_read_b128 v[44:47], v240 offset:51200
	ds_read_b128 v[48:51], v239 offset:53248
	ds_read_b128 v[56:59], v239 offset:55296
	ds_read_b128 v[52:55], v240 offset:53248
	ds_read_b128 v[60:63], v240 offset:55296
	global_load_lds_dwordx4 v[212:213], off
	s_add_i32 m0, s16, 0x2000
	v_lshl_add_u64 v[212:213], s[14:15], 0, v[196:197]
	s_add_u32 s14, s14, 0x20000
	s_addc_u32 s15, s15, 0
	s_add_i32 s16, s17, s20
	global_load_lds_dwordx4 v[212:213], off
	v_lshl_add_u64 v[212:213], s[14:15], 0, v[194:195]
	s_mov_b32 m0, s16
	s_nop 0
	global_load_lds_dwordx4 v[212:213], off
	s_add_i32 m0, s16, 0x2000
	v_lshl_add_u64 v[212:213], s[14:15], 0, v[196:197]
	s_add_u32 s12, s78, s12
	global_load_lds_dwordx4 v[212:213], off
	s_addc_u32 s13, s79, s13
	s_mov_b32 m0, s39
	s_nop 0
	global_load_lds_dwordx4 v202, s[12:13]
	s_mov_b32 m0, s40
	s_nop 0
	global_load_lds_dwordx4 v204, s[12:13]
	s_waitcnt vmcnt(8)
	s_waitcnt lgkmcnt(0)
	s_barrier
	s_setprio 1
	s_waitcnt lgkmcnt(0)
	v_mfma_scale_f32_16x16x128_f8f6f4 v[126:129], v[0:7], v[32:39], v[126:129], v226, v225 op_sel_hi:[0,0,0]
	v_mfma_scale_f32_16x16x128_f8f6f4 v[122:125], v[8:15], v[32:39], v[122:125], v226, v225 op_sel_hi:[0,0,0]
	v_mfma_scale_f32_16x16x128_f8f6f4 v[110:113], v[0:7], v[40:47], v[110:113], v226, v225 op_sel_hi:[0,0,0]
	v_mfma_scale_f32_16x16x128_f8f6f4 v[106:109], v[8:15], v[40:47], v[106:109], v226, v225 op_sel_hi:[0,0,0]
	v_mfma_scale_f32_16x16x128_f8f6f4 v[92:95], v[0:7], v[48:55], v[92:95], v226, v225 op_sel_hi:[0,0,0]
	v_mfma_scale_f32_16x16x128_f8f6f4 v[88:91], v[8:15], v[48:55], v[88:91], v226, v225 op_sel_hi:[0,0,0]
	v_mfma_scale_f32_16x16x128_f8f6f4 v[76:79], v[0:7], v[56:63], v[76:79], v226, v225 op_sel_hi:[0,0,0]
	v_mfma_scale_f32_16x16x128_f8f6f4 v[72:75], v[8:15], v[56:63], v[72:75], v226, v225 op_sel_hi:[0,0,0]
	s_setprio 0
	s_setprio 1
	v_mfma_scale_f32_16x16x128_f8f6f4 v[118:121], v[16:23], v[32:39], v[118:121], v226, v225 op_sel_hi:[0,0,0]
	v_mfma_scale_f32_16x16x128_f8f6f4 v[114:117], v[24:31], v[32:39], v[114:117], v226, v225 op_sel_hi:[0,0,0]
	v_mfma_scale_f32_16x16x128_f8f6f4 v[102:105], v[16:23], v[40:47], v[102:105], v226, v225 op_sel_hi:[0,0,0]
	v_mfma_scale_f32_16x16x128_f8f6f4 v[98:101], v[24:31], v[40:47], v[98:101], v226, v225 op_sel_hi:[0,0,0]
	v_mfma_scale_f32_16x16x128_f8f6f4 v[84:87], v[16:23], v[48:55], v[84:87], v226, v225 op_sel_hi:[0,0,0]
	v_mfma_scale_f32_16x16x128_f8f6f4 v[80:83], v[24:31], v[48:55], v[80:83], v226, v225 op_sel_hi:[0,0,0]
	v_mfma_scale_f32_16x16x128_f8f6f4 v[68:71], v[16:23], v[56:63], v[68:71], v226, v225 op_sel_hi:[0,0,0]
	v_mfma_scale_f32_16x16x128_f8f6f4 v[64:67], v[24:31], v[56:63], v[64:67], v226, v225 op_sel_hi:[0,0,0]
	s_setprio 0
	s_barrier
	s_add_u32 s10, s10, 0x100
	s_addc_u32 s11, s11, 0
	s_cmp_gt_u32 s49, 5
	s_cbranch_scc1 .LBB0_991
	s_mov_b32 s49, s52
	s_branch .LBB0_986

.LBB0_1267:
	s_cmpk_eq_i32 s16, 0x300
	s_cselect_b64 s[18:19], -1, 0
	s_add_i32 s13, 0, 0x10000
	v_add_u32_e32 v0, s13, v209
	s_add_i32 s20, 0, 0x14000
	v_add_u32_e32 v1, s13, v239
	ds_read_b128 v[8:11], v0
	ds_read_b128 v[12:15], v1
	v_add_u32_e32 v0, s76, v209
	v_add_u32_e32 v1, s76, v239
	ds_read_b128 v[24:27], v0
	ds_read_b128 v[28:31], v1
	v_add_u32_e32 v0, s20, v209
	v_add_u32_e32 v4, s20, v239
	v_add_u32_e32 v16, s77, v209
	v_add_u32_e32 v20, s77, v239
	ds_read_b128 v[0:3], v0
	ds_read_b128 v[4:7], v4
	ds_read_b128 v[16:19], v16
	ds_read_b128 v[20:23], v20
	s_add_i32 m0, s40, 0xc000
	s_add_u32 s20, s65, s16
	s_addc_u32 s21, s80, s17
	s_add_i32 s13, s40, 0xe000
	s_cmpk_lg_i32 s16, 0x300
	ds_read_b128 v[40:43], v244
	ds_read_b128 v[32:35], v244 offset:2048
	ds_read_b128 v[44:47], v245
	ds_read_b128 v[36:39], v245 offset:2048
	ds_read_b128 v[56:59], v244 offset:4096
	ds_read_b128 v[48:51], v244 offset:6144
	ds_read_b128 v[60:63], v245 offset:4096
	ds_read_b128 v[52:55], v245 offset:6144
	global_load_lds_dwordx4 v96, s[20:21]
	s_mov_b32 m0, s13
	s_nop 0
	global_load_lds_dwordx4 v204, s[20:21]
	s_waitcnt vmcnt(8)
	s_waitcnt lgkmcnt(0)
	s_barrier
	s_setprio 1
	s_waitcnt lgkmcnt(0)
	v_mfma_scale_f32_16x16x128_f8f6f4 v[72:75], v[8:15], v[40:47], v[72:75], v226, v225 op_sel_hi:[0,0,0]
	v_mfma_scale_f32_16x16x128_f8f6f4 v[64:67], v[24:31], v[40:47], v[64:67], v226, v225 op_sel_hi:[0,0,0]
	v_mfma_scale_f32_16x16x128_f8f6f4 v[88:91], v[8:15], v[32:39], v[88:91], v226, v225 op_sel_hi:[0,0,0]
	v_mfma_scale_f32_16x16x128_f8f6f4 v[80:83], v[24:31], v[32:39], v[80:83], v226, v225 op_sel_hi:[0,0,0]
	v_mfma_scale_f32_16x16x128_f8f6f4 v[126:129], v[8:15], v[56:63], v[126:129], v226, v225 op_sel_hi:[0,0,0]
	v_mfma_scale_f32_16x16x128_f8f6f4 v[106:109], v[24:31], v[56:63], v[106:109], v226, v225 op_sel_hi:[0,0,0]
	v_mfma_scale_f32_16x16x128_f8f6f4 v[158:161], v[8:15], v[48:55], v[158:161], v226, v225 op_sel_hi:[0,0,0]
	v_mfma_scale_f32_16x16x128_f8f6f4 v[142:145], v[24:31], v[48:55], v[142:145], v226, v225 op_sel_hi:[0,0,0]
	s_setprio 0
	s_setprio 1
	v_mfma_scale_f32_16x16x128_f8f6f4 v[76:79], v[0:7], v[40:47], v[76:79], v226, v225 op_sel_hi:[0,0,0]
	v_mfma_scale_f32_16x16x128_f8f6f4 v[68:71], v[16:23], v[40:47], v[68:71], v226, v225 op_sel_hi:[0,0,0]
	v_mfma_scale_f32_16x16x128_f8f6f4 v[102:105], v[0:7], v[32:39], v[102:105], v226, v225 op_sel_hi:[0,0,0]
	v_mfma_scale_f32_16x16x128_f8f6f4 v[84:87], v[16:23], v[32:39], v[84:87], v226, v225 op_sel_hi:[0,0,0]
	v_mfma_scale_f32_16x16x128_f8f6f4 v[134:137], v[0:7], v[56:63], v[134:137], v226, v225 op_sel_hi:[0,0,0]
	v_mfma_scale_f32_16x16x128_f8f6f4 v[118:121], v[16:23], v[56:63], v[118:121], v226, v225 op_sel_hi:[0,0,0]
	v_mfma_scale_f32_16x16x128_f8f6f4 v[166:169], v[0:7], v[48:55], v[166:169], v226, v225 op_sel_hi:[0,0,0]
	v_mfma_scale_f32_16x16x128_f8f6f4 v[150:153], v[16:23], v[48:55], v[150:153], v226, v225 op_sel_hi:[0,0,0]
	s_setprio 0
	s_barrier
	s_cbranch_scc1 .LBB0_1269
	v_mov_b64_e32 v[214:215], v[212:213]
	v_mov_b64_e32 v[216:217], v[210:211]
	v_mov_b32_e32 v204, v212
	v_mov_b32_e32 v96, v210
	v_mov_b32_e32 v206, v224
	v_mov_b32_e32 v208, v250
	v_mov_b32_e32 v246, v212
	v_mov_b32_e32 v247, v210
	s_branch .LBB0_1270

.LBB0_1270:
	s_and_b64 s[20:21], s[14:15], s[18:19]
	s_add_i32 s13, s11, 2
	s_and_b64 s[18:19], s[18:19], exec
	s_cselect_b32 s96, 0, s13
	s_and_b64 s[18:19], s[20:21], exec
	s_cselect_b32 s18, s10, s12
	s_mul_hi_i32 s19, s18, 0x2aaaaaab
	s_cselect_b32 s20, s81, s93
	s_lshr_b32 s21, s19, 31
	s_add_i32 s19, s19, s21
	s_mul_i32 s21, s19, 6
	s_sub_i32 s18, s18, s21
	s_cmp_lt_u32 s18, 5
	s_cselect_b32 s21, 1, 2
	s_min_u32 s25, s18, 4
	s_add_i32 s24, s18, 1
	s_add_i32 s25, s25, -1
	s_cmp_lt_i32 s18, 3
	s_cselect_b32 s18, 0, s21
	s_cselect_b32 s21, s24, s25
	s_lshl_b32 s19, s19, 2
	s_or_b32 s18, s18, s19
	s_add_i32 s21, s21, s19
	s_cmp_lt_i32 s20, 4
	s_cselect_b32 s18, s18, s21
	s_lshl_b32 s20, s20, 18
	s_ashr_i32 s19, s18, 31
	s_and_b32 s53, s20, 0xc0000
	s_lshl_b64 s[20:21], s[96:97], 7
	s_or_b32 s96, s96, 1
	s_lshl_b64 s[24:25], s[18:19], 20
	s_lshl_b64 s[18:19], s[96:97], 7
	s_add_u32 s24, s31, s24
	s_addc_u32 s25, s38, s25
	s_add_u32 s53, s24, s53
	s_addc_u32 s72, s25, 0
	s_add_u32 s24, s53, s20
	s_addc_u32 s25, s72, s21
	v_lshl_add_u64 v[218:219], s[24:25], 0, v[196:197]
	s_mov_b32 m0, s41
	ds_read_b128 v[56:59], v244 offset:16384
	ds_read_b128 v[60:63], v245 offset:16384
	ds_read_b128 v[48:51], v244 offset:18432
	ds_read_b128 v[52:55], v245 offset:18432
	ds_read_b128 v[40:43], v244 offset:20480
	ds_read_b128 v[44:47], v245 offset:20480
	ds_read_b128 v[32:35], v244 offset:22528
	ds_read_b128 v[36:39], v245 offset:22528
	global_load_lds_dwordx4 v[218:219], off
	v_lshl_add_u64 v[218:219], s[24:25], 0, v[202:203]
	s_add_u32 s24, s24, 0x20000
	s_mov_b32 m0, s45
	s_addc_u32 s25, s25, 0
	global_load_lds_dwordx4 v[218:219], off
	v_lshl_add_u64 v[218:219], s[24:25], 0, v[196:197]
	s_mov_b32 m0, s48
	s_add_u32 s20, s78, s20
	global_load_lds_dwordx4 v[218:219], off
	v_lshl_add_u64 v[218:219], s[24:25], 0, v[202:203]
	s_mov_b32 m0, s49
	s_addc_u32 s21, s79, s21
	global_load_lds_dwordx4 v[218:219], off
	s_mov_b32 m0, s40
	s_nop 0
	global_load_lds_dwordx4 v208, s[20:21]
	s_mov_b32 m0, s57
	s_nop 0
	global_load_lds_dwordx4 v206, s[20:21]
	s_waitcnt vmcnt(8)
	s_waitcnt lgkmcnt(0)
	s_barrier
	s_setprio 1
	s_waitcnt lgkmcnt(0)
	v_mfma_scale_f32_16x16x128_f8f6f4 v[110:113], v[8:15], v[56:63], v[110:113], v226, v225 op_sel_hi:[0,0,0]
	v_mfma_scale_f32_16x16x128_f8f6f4 v[92:95], v[24:31], v[56:63], v[92:95], v226, v225 op_sel_hi:[0,0,0]
	v_mfma_scale_f32_16x16x128_f8f6f4 v[138:141], v[8:15], v[48:55], v[138:141], v226, v225 op_sel_hi:[0,0,0]
	v_mfma_scale_f32_16x16x128_f8f6f4 v[122:125], v[24:31], v[48:55], v[122:125], v226, v225 op_sel_hi:[0,0,0]
	v_mfma_scale_f32_16x16x128_f8f6f4 v[170:173], v[8:15], v[40:47], v[170:173], v226, v225 op_sel_hi:[0,0,0]
	v_mfma_scale_f32_16x16x128_f8f6f4 v[154:157], v[24:31], v[40:47], v[154:157], v226, v225 op_sel_hi:[0,0,0]
	v_mfma_scale_f32_16x16x128_f8f6f4 v[186:189], v[8:15], v[32:39], v[186:189], v226, v225 op_sel_hi:[0,0,0]
	v_mfma_scale_f32_16x16x128_f8f6f4 v[178:181], v[24:31], v[32:39], v[178:181], v226, v225 op_sel_hi:[0,0,0]
	s_setprio 0
	s_setprio 1
	v_mfma_scale_f32_16x16x128_f8f6f4 v[114:117], v[0:7], v[56:63], v[114:117], v226, v225 op_sel_hi:[0,0,0]
	v_mfma_scale_f32_16x16x128_f8f6f4 v[98:101], v[16:23], v[56:63], v[98:101], v226, v225 op_sel_hi:[0,0,0]
	v_mfma_scale_f32_16x16x128_f8f6f4 v[146:149], v[0:7], v[48:55], v[146:149], v226, v225 op_sel_hi:[0,0,0]
	v_mfma_scale_f32_16x16x128_f8f6f4 v[130:133], v[16:23], v[48:55], v[130:133], v226, v225 op_sel_hi:[0,0,0]
	v_mfma_scale_f32_16x16x128_f8f6f4 v[174:177], v[0:7], v[40:47], v[174:177], v226, v225 op_sel_hi:[0,0,0]
	v_mfma_scale_f32_16x16x128_f8f6f4 v[162:165], v[16:23], v[40:47], v[162:165], v226, v225 op_sel_hi:[0,0,0]
	v_mfma_scale_f32_16x16x128_f8f6f4 v[190:193], v[0:7], v[32:39], v[190:193], v226, v225 op_sel_hi:[0,0,0]
	v_mfma_scale_f32_16x16x128_f8f6f4 v[182:185], v[16:23], v[32:39], v[182:185], v226, v225 op_sel_hi:[0,0,0]
	s_setprio 0
	s_barrier
	s_add_i32 s24, 0, 0x18000
	s_add_i32 s25, 0, 0x1c000
	v_add_u32_e32 v0, s24, v209
	v_add_u32_e32 v4, s24, v239
	v_add_u32_e32 v8, s94, v209
	v_add_u32_e32 v12, s94, v239
	v_add_u32_e32 v16, s25, v209
	v_add_u32_e32 v20, s25, v239
	v_add_u32_e32 v24, s33, v209
	v_add_u32_e32 v28, s33, v239
	ds_read_b128 v[0:3], v0
	ds_read_b128 v[4:7], v4
	ds_read_b128 v[8:11], v8
	ds_read_b128 v[12:15], v12
	ds_read_b128 v[16:19], v16
	ds_read_b128 v[20:23], v20
	ds_read_b128 v[24:27], v24
	ds_read_b128 v[28:31], v28
	s_mov_b32 m0, s58
	v_lshl_add_u64 v[216:217], s[20:21], 0, v[216:217]
	ds_read_b128 v[32:35], v244 offset:32768
	ds_read_b128 v[40:43], v244 offset:34816
	ds_read_b128 v[36:39], v245 offset:32768
	ds_read_b128 v[44:47], v245 offset:34816
	ds_read_b128 v[48:51], v244 offset:36864
	ds_read_b128 v[56:59], v244 offset:38912
	ds_read_b128 v[52:55], v245 offset:36864
	ds_read_b128 v[60:63], v245 offset:38912
	global_load_lds_dwordx4 v[216:217], off
	v_lshl_add_u64 v[214:215], s[20:21], 0, v[214:215]
	s_mov_b32 m0, s59
	s_nop 0
	global_load_lds_dwordx4 v[214:215], off
	s_waitcnt vmcnt(8)
	s_waitcnt lgkmcnt(0)
	s_barrier
	s_setprio 1
	s_waitcnt lgkmcnt(0)
	v_mfma_scale_f32_16x16x128_f8f6f4 v[72:75], v[0:7], v[32:39], v[72:75], v226, v225 op_sel_hi:[0,0,0]
	v_mfma_scale_f32_16x16x128_f8f6f4 v[64:67], v[8:15], v[32:39], v[64:67], v226, v225 op_sel_hi:[0,0,0]
	v_mfma_scale_f32_16x16x128_f8f6f4 v[88:91], v[0:7], v[40:47], v[88:91], v226, v225 op_sel_hi:[0,0,0]
	v_mfma_scale_f32_16x16x128_f8f6f4 v[80:83], v[8:15], v[40:47], v[80:83], v226, v225 op_sel_hi:[0,0,0]
	v_mfma_scale_f32_16x16x128_f8f6f4 v[126:129], v[0:7], v[48:55], v[126:129], v226, v225 op_sel_hi:[0,0,0]
	v_mfma_scale_f32_16x16x128_f8f6f4 v[106:109], v[8:15], v[48:55], v[106:109], v226, v225 op_sel_hi:[0,0,0]
	v_mfma_scale_f32_16x16x128_f8f6f4 v[158:161], v[0:7], v[56:63], v[158:161], v226, v225 op_sel_hi:[0,0,0]
	v_mfma_scale_f32_16x16x128_f8f6f4 v[142:145], v[8:15], v[56:63], v[142:145], v226, v225 op_sel_hi:[0,0,0]
	s_setprio 0
	s_setprio 1
	v_mfma_scale_f32_16x16x128_f8f6f4 v[76:79], v[16:23], v[32:39], v[76:79], v226, v225 op_sel_hi:[0,0,0]
	v_mfma_scale_f32_16x16x128_f8f6f4 v[68:71], v[24:31], v[32:39], v[68:71], v226, v225 op_sel_hi:[0,0,0]
	v_mfma_scale_f32_16x16x128_f8f6f4 v[102:105], v[16:23], v[40:47], v[102:105], v226, v225 op_sel_hi:[0,0,0]
	v_mfma_scale_f32_16x16x128_f8f6f4 v[84:87], v[24:31], v[40:47], v[84:87], v226, v225 op_sel_hi:[0,0,0]
	v_mfma_scale_f32_16x16x128_f8f6f4 v[134:137], v[16:23], v[48:55], v[134:137], v226, v225 op_sel_hi:[0,0,0]
	v_mfma_scale_f32_16x16x128_f8f6f4 v[118:121], v[24:31], v[48:55], v[118:121], v226, v225 op_sel_hi:[0,0,0]
	v_mfma_scale_f32_16x16x128_f8f6f4 v[166:169], v[16:23], v[56:63], v[166:169], v226, v225 op_sel_hi:[0,0,0]
	v_mfma_scale_f32_16x16x128_f8f6f4 v[150:153], v[24:31], v[56:63], v[150:153], v226, v225 op_sel_hi:[0,0,0]
	s_setprio 0
	s_barrier
	s_add_u32 s20, s53, s18
	s_addc_u32 s21, s72, s19
	s_add_i32 s24, s24, s39
	v_lshl_add_u64 v[214:215], s[20:21], 0, v[196:197]
	s_mov_b32 m0, s24
	ds_read_b128 v[32:35], v244 offset:49152
	ds_read_b128 v[40:43], v244 offset:51200
	ds_read_b128 v[36:39], v245 offset:49152
	ds_read_b128 v[44:47], v245 offset:51200
	ds_read_b128 v[48:51], v244 offset:53248
	ds_read_b128 v[56:59], v244 offset:55296
	ds_read_b128 v[52:55], v245 offset:53248
	ds_read_b128 v[60:63], v245 offset:55296
	global_load_lds_dwordx4 v[214:215], off
	s_add_i32 m0, s24, 0x2000
	v_lshl_add_u64 v[214:215], s[20:21], 0, v[202:203]
	s_add_u32 s20, s20, 0x20000
	s_addc_u32 s21, s21, 0
	s_add_i32 s24, s25, s39
	global_load_lds_dwordx4 v[214:215], off
	v_lshl_add_u64 v[214:215], s[20:21], 0, v[196:197]
	s_mov_b32 m0, s24
	s_nop 0
	global_load_lds_dwordx4 v[214:215], off
	s_add_i32 m0, s24, 0x2000
	v_lshl_add_u64 v[214:215], s[20:21], 0, v[202:203]
	s_add_u32 s18, s78, s18
	global_load_lds_dwordx4 v[214:215], off
	s_addc_u32 s19, s79, s19
	s_mov_b32 m0, s60
	s_nop 0
	global_load_lds_dwordx4 v208, s[18:19]
	s_mov_b32 m0, s61
	s_nop 0
	global_load_lds_dwordx4 v206, s[18:19]
	s_waitcnt vmcnt(8)
	s_waitcnt lgkmcnt(0)
	s_barrier
	s_setprio 1
	s_waitcnt lgkmcnt(0)
	v_mfma_scale_f32_16x16x128_f8f6f4 v[110:113], v[0:7], v[32:39], v[110:113], v226, v225 op_sel_hi:[0,0,0]
	v_mfma_scale_f32_16x16x128_f8f6f4 v[92:95], v[8:15], v[32:39], v[92:95], v226, v225 op_sel_hi:[0,0,0]
	v_mfma_scale_f32_16x16x128_f8f6f4 v[138:141], v[0:7], v[40:47], v[138:141], v226, v225 op_sel_hi:[0,0,0]
	v_mfma_scale_f32_16x16x128_f8f6f4 v[122:125], v[8:15], v[40:47], v[122:125], v226, v225 op_sel_hi:[0,0,0]
	v_mfma_scale_f32_16x16x128_f8f6f4 v[170:173], v[0:7], v[48:55], v[170:173], v226, v225 op_sel_hi:[0,0,0]
	v_mfma_scale_f32_16x16x128_f8f6f4 v[154:157], v[8:15], v[48:55], v[154:157], v226, v225 op_sel_hi:[0,0,0]
	v_mfma_scale_f32_16x16x128_f8f6f4 v[186:189], v[0:7], v[56:63], v[186:189], v226, v225 op_sel_hi:[0,0,0]
	v_mfma_scale_f32_16x16x128_f8f6f4 v[178:181], v[8:15], v[56:63], v[178:181], v226, v225 op_sel_hi:[0,0,0]
	s_setprio 0
	s_setprio 1
	v_mfma_scale_f32_16x16x128_f8f6f4 v[114:117], v[16:23], v[32:39], v[114:117], v226, v225 op_sel_hi:[0,0,0]
	v_mfma_scale_f32_16x16x128_f8f6f4 v[98:101], v[24:31], v[32:39], v[98:101], v226, v225 op_sel_hi:[0,0,0]
	v_mfma_scale_f32_16x16x128_f8f6f4 v[146:149], v[16:23], v[40:47], v[146:149], v226, v225 op_sel_hi:[0,0,0]
	v_mfma_scale_f32_16x16x128_f8f6f4 v[130:133], v[24:31], v[40:47], v[130:133], v226, v225 op_sel_hi:[0,0,0]
	v_mfma_scale_f32_16x16x128_f8f6f4 v[174:177], v[16:23], v[48:55], v[174:177], v226, v225 op_sel_hi:[0,0,0]
	v_mfma_scale_f32_16x16x128_f8f6f4 v[162:165], v[24:31], v[48:55], v[162:165], v226, v225 op_sel_hi:[0,0,0]
	v_mfma_scale_f32_16x16x128_f8f6f4 v[190:193], v[16:23], v[56:63], v[190:193], v226, v225 op_sel_hi:[0,0,0]
	v_mfma_scale_f32_16x16x128_f8f6f4 v[182:185], v[24:31], v[56:63], v[182:185], v226, v225 op_sel_hi:[0,0,0]
	s_setprio 0
	s_barrier
	s_add_u32 s16, s16, 0x100
	s_addc_u32 s17, s17, 0
	s_cmp_gt_u32 s11, 5
	s_cbranch_scc1 .LBB0_1272
	s_mov_b32 s11, s13
	s_branch .LBB0_1267

.LBB0_1502:
	s_add_i32 s15, 0, 0x10000
	v_add_u32_e32 v0, s15, v197
	v_add_u32_e32 v4, s15, v237
	v_add_u32_e32 v8, s76, v197
	s_add_i32 s15, 0, 0x14000
	ds_read_b128 v[0:3], v0
	ds_read_b128 v[4:7], v4
	v_add_u32_e32 v9, s76, v237
	ds_read_b128 v[16:19], v8
	ds_read_b128 v[20:23], v9
	v_add_u32_e32 v8, s15, v197
	v_add_u32_e32 v12, s15, v237
	v_add_u32_e32 v24, s77, v197
	v_add_u32_e32 v28, s77, v237
	ds_read_b128 v[8:11], v8
	ds_read_b128 v[12:15], v12
	ds_read_b128 v[24:27], v24
	ds_read_b128 v[28:31], v28
	s_or_b32 s96, s13, 1
	s_lshl_b64 s[38:39], s[96:97], 7
	s_add_u32 s38, s34, s38
	s_addc_u32 s39, s35, s39
	s_add_i32 m0, s11, 0xc000
	ds_read_b128 v[40:43], v248
	ds_read_b128 v[32:35], v248 offset:2048
	ds_read_b128 v[44:47], v249
	ds_read_b128 v[36:39], v249 offset:2048
	ds_read_b128 v[56:59], v248 offset:4096
	ds_read_b128 v[48:51], v248 offset:6144
	ds_read_b128 v[60:63], v249 offset:4096
	ds_read_b128 v[52:55], v249 offset:6144
	global_load_lds_dwordx4 v96, s[38:39]
	s_add_i32 m0, s11, 0xe000
	s_nop 0
	global_load_lds_dwordx4 v202, s[38:39]
	s_waitcnt vmcnt(8)
	s_waitcnt lgkmcnt(0)
	s_barrier
	s_setprio 1
	s_waitcnt lgkmcnt(0)
	v_mfma_scale_f32_16x16x128_f8f6f4 v[190:193], v[0:7], v[40:47], v[190:193], v226, v228 op_sel_hi:[0,0,0]
	v_mfma_scale_f32_16x16x128_f8f6f4 v[186:189], v[16:23], v[40:47], v[186:189], v226, v228 op_sel_hi:[0,0,0]
	v_mfma_scale_f32_16x16x128_f8f6f4 v[182:185], v[0:7], v[32:39], v[182:185], v226, v228 op_sel_hi:[0,0,0]
	v_mfma_scale_f32_16x16x128_f8f6f4 v[178:181], v[16:23], v[32:39], v[178:181], v226, v228 op_sel_hi:[0,0,0]
	v_mfma_scale_f32_16x16x128_f8f6f4 v[174:177], v[0:7], v[56:63], v[174:177], v226, v228 op_sel_hi:[0,0,0]
	v_mfma_scale_f32_16x16x128_f8f6f4 v[170:173], v[16:23], v[56:63], v[170:173], v226, v228 op_sel_hi:[0,0,0]
	v_mfma_scale_f32_16x16x128_f8f6f4 v[166:169], v[0:7], v[48:55], v[166:169], v226, v228 op_sel_hi:[0,0,0]
	v_mfma_scale_f32_16x16x128_f8f6f4 v[154:157], v[16:23], v[48:55], v[154:157], v226, v228 op_sel_hi:[0,0,0]
	s_setprio 0
	s_setprio 1
	v_mfma_scale_f32_16x16x128_f8f6f4 v[162:165], v[8:15], v[40:47], v[162:165], v226, v228 op_sel_hi:[0,0,0]
	v_mfma_scale_f32_16x16x128_f8f6f4 v[158:161], v[24:31], v[40:47], v[158:161], v226, v228 op_sel_hi:[0,0,0]
	v_mfma_scale_f32_16x16x128_f8f6f4 v[150:153], v[8:15], v[32:39], v[150:153], v226, v228 op_sel_hi:[0,0,0]
	v_mfma_scale_f32_16x16x128_f8f6f4 v[146:149], v[24:31], v[32:39], v[146:149], v226, v228 op_sel_hi:[0,0,0]
	v_mfma_scale_f32_16x16x128_f8f6f4 v[142:145], v[8:15], v[56:63], v[142:145], v226, v228 op_sel_hi:[0,0,0]
	v_mfma_scale_f32_16x16x128_f8f6f4 v[138:141], v[24:31], v[56:63], v[138:141], v226, v228 op_sel_hi:[0,0,0]
	v_mfma_scale_f32_16x16x128_f8f6f4 v[134:137], v[8:15], v[48:55], v[134:137], v226, v228 op_sel_hi:[0,0,0]
	v_mfma_scale_f32_16x16x128_f8f6f4 v[130:133], v[24:31], v[48:55], v[130:133], v226, v228 op_sel_hi:[0,0,0]
	s_setprio 0
	s_barrier
	s_andn2_b64 vcc, exec, s[30:31]
	s_cbranch_vccnz .LBB0_1504
	v_mov_b64_e32 v[212:213], v[208:209]
	v_mov_b64_e32 v[214:215], v[210:211]
	v_mov_b32_e32 v202, v208
	v_mov_b32_e32 v96, v210
	v_mov_b32_e32 v196, v224
	v_mov_b32_e32 v194, v236
	v_mov_b32_e32 v250, v208
	v_mov_b32_e32 v251, v210
	s_branch .LBB0_1505

.LBB0_1505:
	s_add_i32 s15, s13, 2
	s_and_b64 s[30:31], s[30:31], exec
	s_cselect_b32 s96, 0, s15
	s_and_b64 s[30:31], s[28:29], exec
	s_cselect_b32 s30, s80, s14
	s_mul_hi_i32 s31, s30, 0x2aaaaaab
	s_lshr_b32 s38, s31, 31
	s_add_i32 s31, s31, s38
	s_mul_i32 s38, s31, 6
	s_sub_i32 s30, s30, s38
	s_cmp_lt_u32 s30, 5
	s_cselect_b32 s38, 1, 2
	s_min_u32 s40, s30, 4
	s_add_i32 s39, s30, 1
	s_add_i32 s40, s40, -1
	s_cmp_lt_i32 s30, 3
	s_cselect_b32 s30, 0, s38
	s_cselect_b32 s38, s39, s40
	s_lshl_b32 s31, s31, 2
	s_or_b32 s30, s30, s31
	s_add_i32 s38, s38, s31
	s_cmp_lt_u32 s96, 4
	s_cselect_b32 s30, s30, s38
	s_ashr_i32 s31, s30, 31
	s_and_b64 s[28:29], s[28:29], exec
	s_cselect_b32 s28, s20, s10
	s_ashr_i32 s29, s28, 31
	s_lshl_b64 s[38:39], s[28:29], 17
	s_lshl_b32 s28, s96, 7
	s_and_b32 s40, s28, 0x100
	s_or_b32 s28, s96, 1
	s_lshl_b32 s29, s28, 7
	s_lshl_b64 s[30:31], s[30:31], 19
	s_and_b32 s29, s29, 0x180
	s_add_u32 s30, s59, s30
	s_addc_u32 s31, s60, s31
	s_add_u32 s38, s30, s38
	s_addc_u32 s39, s31, s39
	s_add_u32 s30, s38, s40
	s_addc_u32 s31, s39, 0
	v_lshl_add_u64 v[216:217], s[30:31], 0, v[204:205]
	s_mov_b32 m0, s92
	ds_read_b128 v[56:59], v248 offset:16384
	ds_read_b128 v[60:63], v249 offset:16384
	ds_read_b128 v[48:51], v248 offset:18432
	ds_read_b128 v[52:55], v249 offset:18432
	ds_read_b128 v[40:43], v248 offset:20480
	ds_read_b128 v[44:47], v249 offset:20480
	ds_read_b128 v[32:35], v248 offset:22528
	ds_read_b128 v[36:39], v249 offset:22528
	global_load_lds_dwordx4 v[216:217], off
	v_lshl_add_u64 v[216:217], s[30:31], 0, v[206:207]
	s_add_u32 s30, s30, 0x10000
	s_mov_b32 m0, s61
	s_addc_u32 s31, s31, 0
	global_load_lds_dwordx4 v[216:217], off
	v_lshl_add_u64 v[216:217], s[30:31], 0, v[204:205]
	s_mov_b32 m0, s64
	s_nop 0
	global_load_lds_dwordx4 v[216:217], off
	v_lshl_add_u64 v[216:217], s[30:31], 0, v[206:207]
	s_lshl_b64 s[30:31], s[96:97], 7
	s_mov_b32 m0, s45
	s_add_u32 s30, s34, s30
	global_load_lds_dwordx4 v[216:217], off
	s_addc_u32 s31, s35, s31
	s_mov_b32 m0, s11
	s_nop 0
	global_load_lds_dwordx4 v194, s[30:31]
	s_mov_b32 m0, s79
	s_nop 0
	global_load_lds_dwordx4 v196, s[30:31]
	s_waitcnt vmcnt(8)
	s_waitcnt lgkmcnt(0)
	s_barrier
	s_setprio 1
	s_waitcnt lgkmcnt(0)
	v_mfma_scale_f32_16x16x128_f8f6f4 v[126:129], v[0:7], v[56:63], v[126:129], v226, v228 op_sel_hi:[0,0,0]
	v_mfma_scale_f32_16x16x128_f8f6f4 v[122:125], v[16:23], v[56:63], v[122:125], v226, v228 op_sel_hi:[0,0,0]
	v_mfma_scale_f32_16x16x128_f8f6f4 v[118:121], v[0:7], v[48:55], v[118:121], v226, v228 op_sel_hi:[0,0,0]
	v_mfma_scale_f32_16x16x128_f8f6f4 v[114:117], v[16:23], v[48:55], v[114:117], v226, v228 op_sel_hi:[0,0,0]
	v_mfma_scale_f32_16x16x128_f8f6f4 v[110:113], v[0:7], v[40:47], v[110:113], v226, v228 op_sel_hi:[0,0,0]
	v_mfma_scale_f32_16x16x128_f8f6f4 v[106:109], v[16:23], v[40:47], v[106:109], v226, v228 op_sel_hi:[0,0,0]
	v_mfma_scale_f32_16x16x128_f8f6f4 v[102:105], v[0:7], v[32:39], v[102:105], v226, v228 op_sel_hi:[0,0,0]
	v_mfma_scale_f32_16x16x128_f8f6f4 v[98:101], v[16:23], v[32:39], v[98:101], v226, v228 op_sel_hi:[0,0,0]
	s_setprio 0
	s_setprio 1
	v_mfma_scale_f32_16x16x128_f8f6f4 v[92:95], v[8:15], v[56:63], v[92:95], v226, v228 op_sel_hi:[0,0,0]
	v_mfma_scale_f32_16x16x128_f8f6f4 v[88:91], v[24:31], v[56:63], v[88:91], v226, v228 op_sel_hi:[0,0,0]
	v_mfma_scale_f32_16x16x128_f8f6f4 v[84:87], v[8:15], v[48:55], v[84:87], v226, v228 op_sel_hi:[0,0,0]
	v_mfma_scale_f32_16x16x128_f8f6f4 v[80:83], v[24:31], v[48:55], v[80:83], v226, v228 op_sel_hi:[0,0,0]
	v_mfma_scale_f32_16x16x128_f8f6f4 v[76:79], v[8:15], v[40:47], v[76:79], v226, v228 op_sel_hi:[0,0,0]
	v_mfma_scale_f32_16x16x128_f8f6f4 v[72:75], v[24:31], v[40:47], v[72:75], v226, v228 op_sel_hi:[0,0,0]
	v_mfma_scale_f32_16x16x128_f8f6f4 v[68:71], v[8:15], v[32:39], v[68:71], v226, v228 op_sel_hi:[0,0,0]
	v_mfma_scale_f32_16x16x128_f8f6f4 v[64:67], v[24:31], v[32:39], v[64:67], v226, v228 op_sel_hi:[0,0,0]
	s_setprio 0
	s_barrier
	s_add_i32 s40, 0, 0x18000
	s_add_i32 s41, 0, 0x1c000
	v_add_u32_e32 v0, s40, v197
	v_add_u32_e32 v4, s40, v237
	v_add_u32_e32 v8, s94, v197
	v_add_u32_e32 v12, s94, v237
	v_add_u32_e32 v16, s41, v197
	v_add_u32_e32 v20, s41, v237
	v_add_u32_e32 v24, s33, v197
	v_add_u32_e32 v28, s33, v237
	ds_read_b128 v[0:3], v0
	ds_read_b128 v[4:7], v4
	ds_read_b128 v[8:11], v8
	ds_read_b128 v[12:15], v12
	ds_read_b128 v[16:19], v16
	ds_read_b128 v[20:23], v20
	ds_read_b128 v[24:27], v24
	ds_read_b128 v[28:31], v28
	s_mov_b32 m0, s93
	v_lshl_add_u64 v[214:215], s[30:31], 0, v[214:215]
	ds_read_b128 v[32:35], v248 offset:32768
	ds_read_b128 v[40:43], v248 offset:34816
	ds_read_b128 v[36:39], v249 offset:32768
	ds_read_b128 v[44:47], v249 offset:34816
	ds_read_b128 v[48:51], v248 offset:36864
	ds_read_b128 v[56:59], v248 offset:38912
	ds_read_b128 v[52:55], v249 offset:36864
	ds_read_b128 v[60:63], v249 offset:38912
	global_load_lds_dwordx4 v[214:215], off
	v_lshl_add_u64 v[212:213], s[30:31], 0, v[212:213]
	s_mov_b32 m0, s65
	s_nop 0
	global_load_lds_dwordx4 v[212:213], off
	s_waitcnt vmcnt(8)
	s_waitcnt lgkmcnt(0)
	s_barrier
	s_setprio 1
	s_waitcnt lgkmcnt(0)
	v_mfma_scale_f32_16x16x128_f8f6f4 v[190:193], v[0:7], v[32:39], v[190:193], v226, v228 op_sel_hi:[0,0,0]
	v_mfma_scale_f32_16x16x128_f8f6f4 v[186:189], v[8:15], v[32:39], v[186:189], v226, v228 op_sel_hi:[0,0,0]
	v_mfma_scale_f32_16x16x128_f8f6f4 v[182:185], v[0:7], v[40:47], v[182:185], v226, v228 op_sel_hi:[0,0,0]
	v_mfma_scale_f32_16x16x128_f8f6f4 v[178:181], v[8:15], v[40:47], v[178:181], v226, v228 op_sel_hi:[0,0,0]
	v_mfma_scale_f32_16x16x128_f8f6f4 v[174:177], v[0:7], v[48:55], v[174:177], v226, v228 op_sel_hi:[0,0,0]
	v_mfma_scale_f32_16x16x128_f8f6f4 v[170:173], v[8:15], v[48:55], v[170:173], v226, v228 op_sel_hi:[0,0,0]
	v_mfma_scale_f32_16x16x128_f8f6f4 v[166:169], v[0:7], v[56:63], v[166:169], v226, v228 op_sel_hi:[0,0,0]
	v_mfma_scale_f32_16x16x128_f8f6f4 v[154:157], v[8:15], v[56:63], v[154:157], v226, v228 op_sel_hi:[0,0,0]
	s_setprio 0
	s_setprio 1
	v_mfma_scale_f32_16x16x128_f8f6f4 v[162:165], v[16:23], v[32:39], v[162:165], v226, v228 op_sel_hi:[0,0,0]
	v_mfma_scale_f32_16x16x128_f8f6f4 v[158:161], v[24:31], v[32:39], v[158:161], v226, v228 op_sel_hi:[0,0,0]
	v_mfma_scale_f32_16x16x128_f8f6f4 v[150:153], v[16:23], v[40:47], v[150:153], v226, v228 op_sel_hi:[0,0,0]
	v_mfma_scale_f32_16x16x128_f8f6f4 v[146:149], v[24:31], v[40:47], v[146:149], v226, v228 op_sel_hi:[0,0,0]
	v_mfma_scale_f32_16x16x128_f8f6f4 v[142:145], v[16:23], v[48:55], v[142:145], v226, v228 op_sel_hi:[0,0,0]
	v_mfma_scale_f32_16x16x128_f8f6f4 v[138:141], v[24:31], v[48:55], v[138:141], v226, v228 op_sel_hi:[0,0,0]
	v_mfma_scale_f32_16x16x128_f8f6f4 v[134:137], v[16:23], v[56:63], v[134:137], v226, v228 op_sel_hi:[0,0,0]
	v_mfma_scale_f32_16x16x128_f8f6f4 v[130:133], v[24:31], v[56:63], v[130:133], v226, v228 op_sel_hi:[0,0,0]
	s_setprio 0
	s_barrier
	s_add_u32 s30, s38, s29
	s_addc_u32 s31, s39, 0
	s_add_i32 s29, s40, s78
	v_lshl_add_u64 v[212:213], s[30:31], 0, v[204:205]
	s_mov_b32 m0, s29
	ds_read_b128 v[32:35], v248 offset:49152
	ds_read_b128 v[40:43], v248 offset:51200
	ds_read_b128 v[36:39], v249 offset:49152
	ds_read_b128 v[44:47], v249 offset:51200
	ds_read_b128 v[48:51], v248 offset:53248
	ds_read_b128 v[56:59], v248 offset:55296
	ds_read_b128 v[52:55], v249 offset:53248
	ds_read_b128 v[60:63], v249 offset:55296
	global_load_lds_dwordx4 v[212:213], off
	s_add_i32 m0, s29, 0x2000
	v_lshl_add_u64 v[212:213], s[30:31], 0, v[206:207]
	s_add_u32 s30, s30, 0x10000
	s_addc_u32 s31, s31, 0
	s_add_i32 s29, s41, s78
	global_load_lds_dwordx4 v[212:213], off
	v_lshl_add_u64 v[212:213], s[30:31], 0, v[204:205]
	s_mov_b32 m0, s29
	s_nop 0
	global_load_lds_dwordx4 v[212:213], off
	s_add_i32 m0, s29, 0x2000
	s_mov_b32 s29, s97
	s_lshl_b64 s[28:29], s[28:29], 7
	v_lshl_add_u64 v[212:213], s[30:31], 0, v[206:207]
	s_add_u32 s28, s34, s28
	global_load_lds_dwordx4 v[212:213], off
	s_addc_u32 s29, s35, s29
	s_mov_b32 m0, s81
	s_nop 0
	global_load_lds_dwordx4 v194, s[28:29]
	s_mov_b32 m0, s16
	s_nop 0
	global_load_lds_dwordx4 v196, s[28:29]
	s_waitcnt vmcnt(8)
	s_waitcnt lgkmcnt(0)
	s_barrier
	s_setprio 1
	s_waitcnt lgkmcnt(0)
	v_mfma_scale_f32_16x16x128_f8f6f4 v[126:129], v[0:7], v[32:39], v[126:129], v226, v228 op_sel_hi:[0,0,0]
	v_mfma_scale_f32_16x16x128_f8f6f4 v[122:125], v[8:15], v[32:39], v[122:125], v226, v228 op_sel_hi:[0,0,0]
	v_mfma_scale_f32_16x16x128_f8f6f4 v[118:121], v[0:7], v[40:47], v[118:121], v226, v228 op_sel_hi:[0,0,0]
	v_mfma_scale_f32_16x16x128_f8f6f4 v[114:117], v[8:15], v[40:47], v[114:117], v226, v228 op_sel_hi:[0,0,0]
	v_mfma_scale_f32_16x16x128_f8f6f4 v[110:113], v[0:7], v[48:55], v[110:113], v226, v228 op_sel_hi:[0,0,0]
	v_mfma_scale_f32_16x16x128_f8f6f4 v[106:109], v[8:15], v[48:55], v[106:109], v226, v228 op_sel_hi:[0,0,0]
	v_mfma_scale_f32_16x16x128_f8f6f4 v[102:105], v[0:7], v[56:63], v[102:105], v226, v228 op_sel_hi:[0,0,0]
	v_mfma_scale_f32_16x16x128_f8f6f4 v[98:101], v[8:15], v[56:63], v[98:101], v226, v228 op_sel_hi:[0,0,0]
	s_setprio 0
	s_setprio 1
	v_mfma_scale_f32_16x16x128_f8f6f4 v[92:95], v[16:23], v[32:39], v[92:95], v226, v228 op_sel_hi:[0,0,0]
	v_mfma_scale_f32_16x16x128_f8f6f4 v[88:91], v[24:31], v[32:39], v[88:91], v226, v228 op_sel_hi:[0,0,0]
	v_mfma_scale_f32_16x16x128_f8f6f4 v[84:87], v[16:23], v[40:47], v[84:87], v226, v228 op_sel_hi:[0,0,0]
	v_mfma_scale_f32_16x16x128_f8f6f4 v[80:83], v[24:31], v[40:47], v[80:83], v226, v228 op_sel_hi:[0,0,0]
	v_mfma_scale_f32_16x16x128_f8f6f4 v[76:79], v[16:23], v[48:55], v[76:79], v226, v228 op_sel_hi:[0,0,0]
	v_mfma_scale_f32_16x16x128_f8f6f4 v[72:75], v[24:31], v[48:55], v[72:75], v226, v228 op_sel_hi:[0,0,0]
	v_mfma_scale_f32_16x16x128_f8f6f4 v[68:71], v[16:23], v[56:63], v[68:71], v226, v228 op_sel_hi:[0,0,0]
	v_mfma_scale_f32_16x16x128_f8f6f4 v[64:67], v[24:31], v[56:63], v[64:67], v226, v228 op_sel_hi:[0,0,0]
	s_setprio 0
	s_barrier
	s_cmp_gt_u32 s13, 5
	s_cbranch_scc1 .LBB0_1507
	s_mov_b32 s13, s15
	s_branch .LBB0_1475
